# v65 + in-proj tile order: the LayerNorm-statistics gelu tiles (2,3) swapped with rope tiles (4,5) so the weight-converting workgroups get cheaper epilogues
# speedup vs baseline: 1.0201x; 1.0156x over previous
;     __device__ bool next(int i, Unit& u) const { if (!base.next(i >> 1, u)) return false; if (i & 1) { u.pm += MTOK / BM; u.pn += DM / BM; } return true; }
;   __device__ __forceinline__ bool next(int i,AttnUnit&u)const{ if(i>=2||vcu>=256)return false; const int s=vcu&3; u.bh=vcu>>2; u.qb=(i==0)?7-s:s; return true; }
;     __host__ __device__ bool next(int i, Unit& u) const {
;         const int L = i * G + c; if (L >= nwg) return false;
;         int wgid = L; { const int q = nwg / NXCD, r = nwg % NXCD, xcd = wgid % NXCD, off = wgid / NXCD; wgid = (xcd < r ? xcd * (q + 1) : r * (q + 1) + (xcd - r) * q) + off; }
;         const int nig = WGM * nN, gid = wgid / nig, fm = gid * WGM, gsz = (nM - fm) < WGM ? (nM - fm) : WGM;
;         u.pm = fm + ((wgid % nig) % gsz); u.pn = (wgid % nig) / gsz; u.half = 0; return true;
.LBB0_382:
	s_ashr_i32 s4, s21, 31
	s_lshr_b32 s4, s4, 29
	s_add_i32 s4, s21, s4
	s_ashr_i32 s5, s4, 3
	s_and_b32 s4, s4, -8
	s_sub_i32 s4, s21, s4
	s_cmp_lt_i32 s4, 0
	s_movk_i32 s6, 0x91
	s_cselect_b32 s6, s6, 0x90
	s_mul_i32 s4, s4, s6
	s_add_i32 s4, s4, s5
	s_mul_hi_i32 s5, s4, 0x38e38e39
	s_lshr_b32 s6, s5, 31
	s_ashr_i32 s5, s5, 5
	s_add_i32 s5, s5, s6
	s_lshl_b32 s6, s5, 3
	s_mulk_i32 s5, 0x90
	s_sub_i32 s4, s4, s5
	s_bfe_u32 s5, s4, 0x3001c
	s_add_i32 s5, s4, s5
	s_sext_i32_i16 s7, s5
	s_and_b32 s5, s5, 0xfff8
	s_sub_i32 s4, s4, s5
	s_sext_i32_i16 s4, s4
	s_add_i32 s18, s6, s4
	s_ashr_i32 s70, s7, 3
	s_mul_i32 s4, s70, 5
	s_cmp_lt_u32 s70, 12
	s_cbranch_scc0 .Lpn_hi0
	s_mov_b32 s6, 0x86229020
	s_mov_b32 s7, 0x5a92839
	s_branch .Lpn_go0
.Lpn_hi0:
	s_sub_i32 s4, s4, 60
	s_mov_b32 s6, 0x2307b9ac
	s_mov_b32 s7, 0

;     __device__ bool next(int i, Unit& u) const { if (!base.next(i >> 1, u)) return false; if (i & 1) { u.pm += MTOK / BM; u.pn += DM / BM; } return true; }
;   __device__ __forceinline__ bool next(int i,AttnUnit&u)const{ if(i>=2||vcu>=256)return false; const int s=vcu&3; u.bh=vcu>>2; u.qb=(i==0)?7-s:s; return true; }
;     __host__ __device__ bool next(int i, Unit& u) const {
;         const int L = i * G + c; if (L >= nwg) return false;
;         int wgid = L; { const int q = nwg / NXCD, r = nwg % NXCD, xcd = wgid % NXCD, off = wgid / NXCD; wgid = (xcd < r ? xcd * (q + 1) : r * (q + 1) + (xcd - r) * q) + off; }
;         const int nig = WGM * nN, gid = wgid / nig, fm = gid * WGM, gsz = (nM - fm) < WGM ? (nM - fm) : WGM;
;         u.pm = fm + ((wgid % nig) % gsz); u.pn = (wgid % nig) / gsz; u.half = 0; return true;
; template <class Epi, class Sched, bool ALIGN_EPI = false, bool SP2 = false>
; __device__ __forceinline__ void gemm_phase(PG8_LAS unsigned char* lds, const Gemm g, const Sched& S, const Epi& E) {
;     ...
;         const bool has_next = S.next(ui + 1, nxt);
;         const char* nA = has_next ? (const char*)g.A + (size_t)nxt.pm * tstep + (nxt.half == 2 ? hstep : (size_t)0) : cA; const char* nB = has_next ? (const char*)g.Bt + (size_t)nxt.pn * tstep : cB;
.LBB0_392:
	s_add_i32 s72, s72, 1
	s_mul_i32 s10, s72, s33
	s_add_i32 s10, s10, s21
	s_cmpk_lt_i32 s10, 0x480
	s_cselect_b64 s[64:65], -1, 0
	s_cmpk_gt_i32 s10, 0x47f
	s_cbranch_scc1 .LBB0_394
	s_ashr_i32 s11, s10, 31
	s_lshr_b32 s11, s11, 29
	s_add_i32 s11, s10, s11
	s_ashr_i32 s12, s11, 3
	s_and_b32 s11, s11, -8
	s_sub_i32 s10, s10, s11
	s_cmp_lt_i32 s10, 0
	s_movk_i32 s11, 0x91
	s_cselect_b32 s11, s11, 0x90
	s_mul_i32 s10, s10, s11
	s_add_i32 s10, s10, s12
	s_mul_hi_i32 s11, s10, 0x38e38e39
	s_lshr_b32 s12, s11, 31
	s_ashr_i32 s11, s11, 5
	s_add_i32 s11, s11, s12
	s_lshl_b32 s12, s11, 3
	s_mulk_i32 s11, 0x90
	s_sub_i32 s10, s10, s11
	s_bfe_u32 s11, s10, 0x3001c
	s_add_i32 s11, s10, s11
	s_sext_i32_i16 s13, s11
	s_and_b32 s11, s11, 0xfff8
	s_sub_i32 s10, s10, s11
	s_sext_i32_i16 s10, s10
	s_add_i32 s60, s12, s10
	s_ashr_i32 s62, s13, 3
	s_mul_i32 s10, s62, 5
	s_cmp_lt_u32 s62, 12
	s_cbranch_scc0 .Lpn_hi1
	s_mov_b32 s12, 0x86229020
	s_mov_b32 s13, 0x5a92839
	s_branch .Lpn_go1
.Lpn_hi1:
	s_sub_i32 s10, s10, 60
	s_mov_b32 s12, 0x2307b9ac
	s_mov_b32 s13, 0
